# GU L0-L2 epilogues: drop the vmcnt(0) before the first store (cstep already prefetched before the K-loop; the next unit's first vmcnt(8) still covers the staged tiles)
# baseline (speedup 1.0000x reference)
; __device__ __forceinline__ float fast_sigmoid(float x) { return __builtin_amdgcn_rcpf(1.0f + __expf(-x)); }
;     __device__ __forceinline__ void operator()(const f32x4 (&acc)[2][2][4][2], const Unit& u, int wr, int wc, int fr, int fq) const {
;         const int row0 = u.pm * BM + wr * 64 + fr, col0 = u.pn * HALF + wc * 32 + 8 * fq; const int sl = IN8 ? rt.slot(u.pm) : 0;
;         f32x4 cg[2], cu[2];
; #pragma unroll
;         for (int n = 0; n < 2; ++n) { cg[n] = IN8 ? *(const f32x4*)(cstep + u.pn * BM + wc * 32 + 8 * fq + 4 * n) : (f32x4){1.f, 1.f, 1.f, 1.f}; cu[n] = IN8 ? *(const f32x4*)(cstep + u.pn * BM + HALF + wc * 32 + 8 * fq + 4 * n) : (f32x4){1.f, 1.f, 1.f, 1.f}; }
; #pragma unroll
;         for (int ai = 0; ai < 2; ++ai)
; #pragma unroll
;             for (int m = 0; m < 4; ++m) { const size_t off = (size_t)(row0 + ai * HALF + m * 16) * ldc + col0;
;                 const float rs = IN8 ? rt.tab[sl * 256 + wr * 64 + ai * HALF + m * 16 + fr] : isc;
;                 const float rsn = rs * -1.4426950408889634f, rs2 = rs * rs; (void)rsn; (void)rs2;
;                 float o[8];
; #pragma unroll
;                 for (int n = 0; n < 2; ++n)
; #pragma unroll
;                     for (int e = 0; e < 4; ++e) { const float ga = acc[ai][0][m][n][e], ua = acc[ai][1][m][n][e];
;                         if (IN8) {
;                             const float gq = (float)__float_as_int(ga) * cg[n][e], uq = (float)__float_as_int(ua) * cu[n][e];
;                             const float sg = __builtin_amdgcn_rcpf(1.0f + __builtin_amdgcn_exp2f(gq * rsn));
;                             o[4 * n + e] = (gq * uq) * (sg * rs2); }
;                         else { const float g = ga * rs, up = ua * rs; o[4 * n + e] = g * fast_sigmoid(g) * up; } }
;                 if (F8) { unsigned w0 = 0u, w1 = 0u;
; #pragma unroll
;                     for (int e = 0; e < 8; ++e) o[e] = __builtin_amdgcn_fmed3f(o[e] * H8_SCALE, -448.0f, 448.0f);
;                     w0 = __builtin_amdgcn_cvt_pk_fp8_f32(o[0], o[1], w0, false); w0 = __builtin_amdgcn_cvt_pk_fp8_f32(o[2], o[3], w0, true);
;                     w1 = __builtin_amdgcn_cvt_pk_fp8_f32(o[4], o[5], w1, false); w1 = __builtin_amdgcn_cvt_pk_fp8_f32(o[6], o[7], w1, true);
;                     typedef unsigned u32x2_ __attribute__((ext_vector_type(2))); *(u32x2_*)((unsigned char*)O + off) = (u32x2_){w0, w1}; }
.LBB0_230:
	s_lshl_b32 s24, s63, 8
	s_ashr_i32 s25, s24, 31
	s_nop 0
	v_mov_b32_e32 v142, v226
	v_mov_b32_e32 v143, v227
	v_mov_b32_e32 v144, v228
	v_mov_b32_e32 v145, v229
	v_mov_b32_e32 v138, v230
	v_mov_b32_e32 v139, v231
	v_mov_b32_e32 v140, v232
	v_mov_b32_e32 v141, v233
	v_mov_b32_e32 v134, v234
	v_mov_b32_e32 v135, v235
	v_mov_b32_e32 v136, v236
	v_mov_b32_e32 v137, v237
	s_nop 0
	v_mov_b32_e32 v130, v238
	v_mov_b32_e32 v131, v239
	v_mov_b32_e32 v132, v240
	v_mov_b32_e32 v133, v241
	s_add_i32 s15, s34, 0x20204
	v_cvt_f32_i32_e32 v172, v118
	v_mov_b32_e32 v118, s15
	v_cvt_f32_i32_e32 v173, v119
	ds_read2_b32 v[118:119], v118 offset1:1
	s_add_i32 s17, s34, 0x2020c
	s_add_i32 s24, s34, 0x20214
	s_add_i32 s25, s34, 0x2021c
	v_mov_b32_e32 v169, s17
	v_mov_b32_e32 v171, s24
	v_mov_b32_e32 v178, s25
	ds_read2_b32 v[174:175], v169 offset1:1
	ds_read2_b32 v[176:177], v171 offset1:1
	ds_read_b32 v169, v178
	s_waitcnt lgkmcnt(0)
	v_cmp_eq_u32_e32 vcc, s22, v118
	v_cvt_f32_i32_e32 v127, v127
	v_cvt_f32_i32_e32 v126, v126
	v_cndmask_b32_e64 v118, 0, 1, vcc
	v_cmp_ne_u32_e32 vcc, s22, v119
	v_cvt_f32_i32_e32 v123, v123
	v_cvt_f32_i32_e32 v122, v122
	v_cndmask_b32_e32 v118, 2, v118, vcc
	v_cmp_ne_u32_e32 vcc, s22, v174
	v_cvt_f32_i32_e32 v129, v129
	v_cvt_f32_i32_e32 v128, v128
	v_cndmask_b32_e32 v118, 3, v118, vcc
	v_cmp_ne_u32_e32 vcc, s22, v175
	v_cvt_f32_i32_e32 v125, v125
	v_cvt_f32_i32_e32 v124, v124
	v_cndmask_b32_e32 v118, 4, v118, vcc
	v_cmp_ne_u32_e32 vcc, s22, v176
	v_cvt_f32_i32_e32 v121, v121
	v_cvt_f32_i32_e32 v120, v120
	v_cndmask_b32_e32 v118, 5, v118, vcc
	v_cmp_ne_u32_e32 vcc, s22, v177
	v_cvt_f32_i32_e32 v115, v115
	v_cvt_f32_i32_e32 v114, v114
	v_cndmask_b32_e32 v118, 6, v118, vcc
	v_cmp_ne_u32_e32 vcc, s22, v169
	v_cvt_f32_i32_e32 v117, v117
	v_cvt_f32_i32_e32 v116, v116
	v_cndmask_b32_e32 v118, 7, v118, vcc
	v_lshl_or_b32 v170, s63, 7, v165
	v_readfirstlane_b32 s15, v118
	v_lshl_add_u32 v168, s22, 8, v1
	v_ashrrev_i32_e32 v171, 31, v170
	v_lshl_add_u32 v118, s15, 10, v166
	ds_read2_b32 v[174:175], v118 offset1:16
	v_cvt_f32_i32_e32 v113, v113
	v_cvt_f32_i32_e32 v112, v112
	v_cvt_f32_i32_e32 v107, v107
	v_cvt_f32_i32_e32 v106, v106
	s_waitcnt lgkmcnt(0)
	v_mul_f32_e32 v119, 0xbfb8aa3b, v174
	v_mul_f32_e32 v174, v174, v174
	v_cvt_f32_i32_e32 v109, v109
	v_cvt_f32_i32_e32 v108, v108
	v_cvt_f32_i32_e32 v103, v103
	v_cvt_f32_i32_e32 v102, v102
	v_cvt_f32_i32_e32 v99, v99
	v_cvt_f32_i32_e32 v98, v98
	v_cvt_f32_i32_e32 v105, v105
	v_cvt_f32_i32_e32 v104, v104
	v_cvt_f32_i32_e32 v101, v101
	v_cvt_f32_i32_e32 v100, v100
	v_cvt_f32_i32_e32 v95, v95
	v_cvt_f32_i32_e32 v94, v94
	v_cvt_f32_i32_e32 v91, v91
	v_cvt_f32_i32_e32 v90, v90
	v_cvt_f32_i32_e32 v97, v97
	v_cvt_f32_i32_e32 v96, v96
	v_cvt_f32_i32_e32 v93, v93
	v_cvt_f32_i32_e32 v92, v92
	v_cvt_f32_i32_e32 v87, v87
	v_cvt_f32_i32_e32 v86, v86
	v_cvt_f32_i32_e32 v83, v83
	v_cvt_f32_i32_e32 v82, v82
	v_cvt_f32_i32_e32 v89, v89
	v_cvt_f32_i32_e32 v88, v88
	s_nop 0
	v_pk_mul_f32 v[126:127], v[142:143], v[126:127]
	v_pk_mul_f32 v[122:123], v[138:139], v[122:123]
	v_pk_mul_f32 v[128:129], v[144:145], v[128:129]
	v_pk_mul_f32 v[124:125], v[140:141], v[124:125]
	v_pk_mul_f32 v[172:173], v[134:135], v[172:173]
	v_pk_mul_f32 v[176:177], v[136:137], v[120:121]
	v_mul_f32_e32 v169, v126, v119
	v_mul_f32_e32 v178, v127, v119
	v_pk_mul_f32 v[120:121], v[126:127], v[122:123]
	v_mul_f32_e32 v126, v128, v119
	v_mul_f32_e32 v127, v129, v119
	v_pk_mul_f32 v[122:123], v[128:129], v[124:125]
	v_mul_f32_e32 v124, v172, v119
	v_mul_f32_e32 v125, v173, v119
	v_exp_f32_e32 v129, v169
	v_exp_f32_e32 v169, v178
	v_exp_f32_e32 v126, v126
	v_exp_f32_e32 v127, v127
	v_exp_f32_e32 v124, v124
	v_exp_f32_e32 v125, v125
	v_pk_mul_f32 v[114:115], v[130:131], v[114:115]
	v_mul_f32_e32 v128, v176, v119
	v_pk_mul_f32 v[114:115], v[172:173], v[114:115]
	v_exp_f32_e32 v172, v128
	v_add_f32_e32 v128, 1.0, v129
	v_add_f32_e32 v129, 1.0, v169
	v_add_f32_e32 v126, 1.0, v126
	v_add_f32_e32 v127, 1.0, v127
	v_add_f32_e32 v169, 1.0, v124
	v_add_f32_e32 v173, 1.0, v125
	v_rcp_f32_e32 v124, v128
	v_rcp_f32_e32 v125, v129
	v_rcp_f32_e32 v126, v126
	v_rcp_f32_e32 v127, v127
	v_rcp_f32_e32 v128, v169
	v_rcp_f32_e32 v129, v173
	v_mul_f32_e32 v119, v177, v119
	v_exp_f32_e32 v119, v119
	v_pk_mul_f32 v[124:125], v[174:175], v[124:125] op_sel_hi:[0,1]
	v_pk_mul_f32 v[126:127], v[174:175], v[126:127] op_sel_hi:[0,1]
	v_pk_mul_f32 v[120:121], v[120:121], v[124:125]
	v_pk_mul_f32 v[122:123], v[122:123], v[126:127]
	v_cvt_pk_bf16_f32 v120, v120, v121
	v_cvt_pk_bf16_f32 v121, v122, v123
	v_pk_mul_f32 v[122:123], v[174:175], v[128:129] op_sel_hi:[0,1]
	v_pk_mul_f32 v[114:115], v[114:115], v[122:123]
	v_add_f32_e32 v122, 1.0, v172
	v_add_f32_e32 v119, 1.0, v119
	v_rcp_f32_e32 v124, v122
	v_rcp_f32_e32 v125, v119
	v_cvt_pk_bf16_f32 v122, v114, v115
	v_pk_mul_f32 v[114:115], v[132:133], v[116:117]
	v_mul_f32_e32 v119, 0xbfb8aa3b, v175
	v_pk_mul_f32 v[114:115], v[176:177], v[114:115]
	v_pk_mul_f32 v[116:117], v[174:175], v[124:125] op_sel_hi:[0,1]
	v_cvt_f32_i32_e32 v125, v111
	v_cvt_f32_i32_e32 v124, v110
	v_pk_mul_f32 v[114:115], v[114:115], v[116:117]
	v_lshlrev_b64 v[110:111], 1, v[170:171]
	v_cvt_pk_bf16_f32 v123, v114, v115
	v_mov_b64_e32 v[114:115], s[6:7]
	v_mad_i64_i32 v[116:117], s[24:25], v168, s62, v[114:115]
	v_lshl_add_u64 v[116:117], v[116:117], 0, v[110:111]
	v_pk_mul_f32 v[124:125], v[142:143], v[124:125]
	global_store_dwordx4 v[116:117], v[120:123], off nt
	v_mul_f32_e32 v126, v124, v119
	v_exp_f32_e32 v126, v126
	v_mul_f32_e32 v121, v125, v119
	v_exp_f32_e32 v121, v121
	v_pk_mul_f32 v[112:113], v[144:145], v[112:113]
; __device__ __forceinline__ float fast_sigmoid(float x) { return __builtin_amdgcn_rcpf(1.0f + __expf(-x)); }
;     __device__ __forceinline__ void operator()(const f32x4 (&acc)[2][2][4][2], const Unit& u, int wr, int wc, int fr, int fq) const {
;     ...
;             for (int m = 0; m < 4; ++m) { const size_t off = (size_t)(row0 + ai * HALF + m * 16) * ldc + col0;
;                 const float rs = IN8 ? rt.tab[sl * 256 + wr * 64 + ai * HALF + m * 16 + fr] : isc;
;                 const float rsn = rs * -1.4426950408889634f, rs2 = rs * rs; (void)rsn; (void)rs2;
;                 float o[8];
; #pragma unroll
;                 for (int n = 0; n < 2; ++n)
; #pragma unroll
;                     for (int e = 0; e < 4; ++e) { const float ga = acc[ai][0][m][n][e], ua = acc[ai][1][m][n][e];
;                         if (IN8) {
;                             const float gq = (float)__float_as_int(ga) * cg[n][e], uq = (float)__float_as_int(ua) * cu[n][e];
;                             const float sg = __builtin_amdgcn_rcpf(1.0f + __builtin_amdgcn_exp2f(gq * rsn));
;                             o[4 * n + e] = (gq * uq) * (sg * rs2); }
;                         else { const float g = ga * rs, up = ua * rs; o[4 * n + e] = g * fast_sigmoid(g) * up; } }
;                 if (F8) { unsigned w0 = 0u, w1 = 0u;
; #pragma unroll
;                     for (int e = 0; e < 8; ++e) o[e] = __builtin_amdgcn_fmed3f(o[e] * H8_SCALE, -448.0f, 448.0f);
;                     w0 = __builtin_amdgcn_cvt_pk_fp8_f32(o[0], o[1], w0, false); w0 = __builtin_amdgcn_cvt_pk_fp8_f32(o[2], o[3], w0, true);
;                     w1 = __builtin_amdgcn_cvt_pk_fp8_f32(o[4], o[5], w1, false); w1 = __builtin_amdgcn_cvt_pk_fp8_f32(o[6], o[7], w1, true);
;                     typedef unsigned u32x2_ __attribute__((ext_vector_type(2))); *(u32x2_*)((unsigned char*)O + off) = (u32x2_){w0, w1}; }
;                 else { u32x4 w; w.x = cvt_pk_bf16(o[0], o[1]); w.y = cvt_pk_bf16(o[2], o[3]); w.z = cvt_pk_bf16(o[4], o[5]); w.w = cvt_pk_bf16(o[6], o[7]);
;                     __builtin_nontemporal_store(w, (u32x4*)((bf16_t*)O + off)); } }
	v_add_f32_e32 v120, 1.0, v126
	v_rcp_f32_e32 v120, v120
	v_add_f32_e32 v121, 1.0, v121
	v_rcp_f32_e32 v121, v121
	v_mul_f32_e32 v122, v112, v119
	v_exp_f32_e32 v122, v122
	v_or_b32_e32 v117, 16, v168
	v_mul_f32_e32 v116, v175, v175
	v_pk_mul_f32 v[106:107], v[138:139], v[106:107]
	v_pk_mul_f32 v[120:121], v[116:117], v[120:121] op_sel_hi:[0,1]
	v_pk_mul_f32 v[106:107], v[124:125], v[106:107]
	v_pk_mul_f32 v[108:109], v[140:141], v[108:109]
	v_pk_mul_f32 v[106:107], v[106:107], v[120:121]
	v_pk_mul_f32 v[108:109], v[112:113], v[108:109]
	v_cvt_pk_bf16_f32 v106, v106, v107
	v_add_f32_e32 v107, 1.0, v122
	v_rcp_f32_e32 v120, v107
	v_mul_f32_e32 v107, v113, v119
	v_exp_f32_e32 v107, v107
	v_pk_mul_f32 v[102:103], v[134:135], v[102:103]
	v_pk_mul_f32 v[98:99], v[130:131], v[98:99]
	v_pk_mul_f32 v[104:105], v[136:137], v[104:105]
	v_add_f32_e32 v107, 1.0, v107
	v_rcp_f32_e32 v121, v107
	v_mul_f32_e32 v107, v102, v119
	v_exp_f32_e32 v122, v107
	v_pk_mul_f32 v[98:99], v[102:103], v[98:99]
	v_pk_mul_f32 v[112:113], v[116:117], v[120:121] op_sel_hi:[0,1]
	v_pk_mul_f32 v[108:109], v[108:109], v[112:113]
	v_mul_f32_e32 v112, v104, v119
	v_cvt_pk_bf16_f32 v107, v108, v109
	v_mul_f32_e32 v109, v103, v119
	v_exp_f32_e32 v109, v109
	v_add_f32_e32 v108, 1.0, v122
	v_rcp_f32_e32 v108, v108
	v_exp_f32_e32 v112, v112
	v_add_f32_e32 v109, 1.0, v109
	v_rcp_f32_e32 v109, v109
	v_pk_mul_f32 v[94:95], v[142:143], v[94:95]
	v_pk_mul_f32 v[90:91], v[138:139], v[90:91]
	v_pk_mul_f32 v[92:93], v[140:141], v[92:93]
	v_pk_mul_f32 v[102:103], v[116:117], v[108:109] op_sel_hi:[0,1]
	v_pk_mul_f32 v[98:99], v[98:99], v[102:103]
	v_mul_f32_e32 v103, v105, v119
	v_exp_f32_e32 v103, v103
	v_add_f32_e32 v102, 1.0, v112
	v_rcp_f32_e32 v102, v102
	v_cvt_pk_bf16_f32 v108, v98, v99
	v_add_f32_e32 v103, 1.0, v103
	v_rcp_f32_e32 v103, v103
	v_pk_mul_f32 v[98:99], v[132:133], v[100:101]
	v_pk_mul_f32 v[90:91], v[94:95], v[90:91]
	v_pk_mul_f32 v[98:99], v[104:105], v[98:99]
	v_pk_mul_f32 v[100:101], v[116:117], v[102:103] op_sel_hi:[0,1]
	v_pk_mul_f32 v[98:99], v[98:99], v[100:101]
	v_mad_i64_i32 v[100:101], s[24:25], v117, s62, v[114:115]
	v_cvt_pk_bf16_f32 v109, v98, v99
	ds_read2_b32 v[98:99], v118 offset0:32 offset1:48
	v_lshl_add_u64 v[100:101], v[100:101], 0, v[110:111]
	global_store_dwordx4 v[100:101], v[106:109], off nt
	v_pk_mul_f32 v[86:87], v[134:135], v[86:87]
	v_pk_mul_f32 v[82:83], v[130:131], v[82:83]
	s_waitcnt lgkmcnt(0)
	v_mul_f32_e32 v102, 0xbfb8aa3b, v98
	v_mul_f32_e32 v103, v94, v102
	v_mul_f32_e32 v101, v95, v102
	v_exp_f32_e32 v103, v103
	v_exp_f32_e32 v101, v101
	v_pk_mul_f32 v[94:95], v[144:145], v[96:97]
	v_mul_f32_e32 v98, v98, v98
	v_add_f32_e32 v100, 1.0, v103
	v_add_f32_e32 v101, 1.0, v101
	v_rcp_f32_e32 v100, v100
	v_rcp_f32_e32 v101, v101
	v_mul_f32_e32 v96, v94, v102
	v_exp_f32_e32 v103, v96
	v_pk_mul_f32 v[92:93], v[94:95], v[92:93]
	v_pk_mul_f32 v[96:97], v[98:99], v[100:101] op_sel_hi:[0,1]
	v_pk_mul_f32 v[90:91], v[90:91], v[96:97]
	v_pk_mul_f32 v[88:89], v[136:137], v[88:89]
	v_cvt_pk_bf16_f32 v90, v90, v91
	v_add_f32_e32 v91, 1.0, v103
	v_rcp_f32_e32 v96, v91
	v_mul_f32_e32 v91, v95, v102
	v_exp_f32_e32 v91, v91
	v_pk_mul_f32 v[82:83], v[86:87], v[82:83]
	v_cvt_f32_i32_e32 v85, v85
	v_cvt_f32_i32_e32 v84, v84
	v_add_f32_e32 v91, 1.0, v91
	v_rcp_f32_e32 v97, v91
	v_mul_f32_e32 v91, v86, v102
	v_exp_f32_e32 v100, v91
	v_cvt_f32_i32_e32 v79, v79
	v_pk_mul_f32 v[94:95], v[98:99], v[96:97] op_sel_hi:[0,1]
	v_pk_mul_f32 v[92:93], v[92:93], v[94:95]
	v_mul_f32_e32 v94, v88, v102
	v_cvt_pk_bf16_f32 v91, v92, v93
	v_mul_f32_e32 v93, v87, v102
	v_exp_f32_e32 v93, v93
	v_add_f32_e32 v92, 1.0, v100
	v_rcp_f32_e32 v92, v92
	v_exp_f32_e32 v94, v94
	v_add_f32_e32 v93, 1.0, v93
	v_rcp_f32_e32 v93, v93
	v_cvt_f32_i32_e32 v78, v78
	v_cvt_f32_i32_e32 v75, v75
	v_cvt_f32_i32_e32 v74, v74
	v_pk_mul_f32 v[86:87], v[98:99], v[92:93] op_sel_hi:[0,1]
	v_pk_mul_f32 v[82:83], v[82:83], v[86:87]
	v_mul_f32_e32 v87, v89, v102
	v_exp_f32_e32 v87, v87
	v_add_f32_e32 v86, 1.0, v94
	v_rcp_f32_e32 v86, v86
	v_cvt_pk_bf16_f32 v92, v82, v83
	v_add_f32_e32 v87, 1.0, v87
	v_rcp_f32_e32 v87, v87
	v_pk_mul_f32 v[82:83], v[132:133], v[84:85]
	v_pk_mul_f32 v[78:79], v[142:143], v[78:79]
	v_pk_mul_f32 v[82:83], v[88:89], v[82:83]
	v_pk_mul_f32 v[84:85], v[98:99], v[86:87] op_sel_hi:[0,1]
	v_mul_f32_e32 v86, 0xbfb8aa3b, v99
	v_pk_mul_f32 v[82:83], v[82:83], v[84:85]
	v_mul_f32_e32 v84, v78, v86
	v_mul_f32_e32 v85, v79, v86
	v_exp_f32_e32 v84, v84
	v_exp_f32_e32 v85, v85
	v_cvt_f32_i32_e32 v81, v81
	v_cvt_f32_i32_e32 v80, v80
	v_add_f32_e32 v84, 1.0, v84
	v_pk_mul_f32 v[74:75], v[138:139], v[74:75]
	v_add_f32_e32 v85, 1.0, v85
	v_or_b32_e32 v104, 32, v168
	v_rcp_f32_e32 v84, v84
	v_rcp_f32_e32 v85, v85
	v_pk_mul_f32 v[74:75], v[78:79], v[74:75]
	v_pk_mul_f32 v[78:79], v[144:145], v[80:81]
	v_cvt_pk_bf16_f32 v93, v82, v83
	v_mad_i64_i32 v[82:83], s[24:25], v104, s62, v[114:115]
	v_mul_f32_e32 v80, v78, v86
	v_lshl_add_u64 v[82:83], v[82:83], 0, v[110:111]
	v_exp_f32_e32 v87, v80
	global_store_dwordx4 v[82:83], v[90:93], off nt
	v_or_b32_e32 v83, 48, v168
	v_mul_f32_e32 v82, v99, v99
	v_pk_mul_f32 v[80:81], v[82:83], v[84:85] op_sel_hi:[0,1]
	v_pk_mul_f32 v[74:75], v[74:75], v[80:81]
	v_cvt_f32_i32_e32 v77, v77
	v_cvt_pk_bf16_f32 v74, v74, v75
	v_add_f32_e32 v75, 1.0, v87
	v_rcp_f32_e32 v80, v75
	v_mul_f32_e32 v75, v79, v86
	v_exp_f32_e32 v75, v75
	v_cvt_f32_i32_e32 v76, v76
	v_cvt_f32_i32_e32 v71, v71
	v_cvt_f32_i32_e32 v70, v70
	v_add_f32_e32 v75, 1.0, v75
	v_rcp_f32_e32 v81, v75
	v_pk_mul_f32 v[76:77], v[140:141], v[76:77]
	v_pk_mul_f32 v[70:71], v[134:135], v[70:71]
; __device__ __forceinline__ float fast_sigmoid(float x) { return __builtin_amdgcn_rcpf(1.0f + __expf(-x)); }
;     __device__ __forceinline__ void operator()(const f32x4 (&acc)[2][2][4][2], const Unit& u, int wr, int wc, int fr, int fq) const {
;     ...
;             for (int m = 0; m < 4; ++m) { const size_t off = (size_t)(row0 + ai * HALF + m * 16) * ldc + col0;
;                 const float rs = IN8 ? rt.tab[sl * 256 + wr * 64 + ai * HALF + m * 16 + fr] : isc;
;                 const float rsn = rs * -1.4426950408889634f, rs2 = rs * rs; (void)rsn; (void)rs2;
;                 float o[8];
; #pragma unroll
;                 for (int n = 0; n < 2; ++n)
; #pragma unroll
;                     for (int e = 0; e < 4; ++e) { const float ga = acc[ai][0][m][n][e], ua = acc[ai][1][m][n][e];
;                         if (IN8) {
;                             const float gq = (float)__float_as_int(ga) * cg[n][e], uq = (float)__float_as_int(ua) * cu[n][e];
;                             const float sg = __builtin_amdgcn_rcpf(1.0f + __builtin_amdgcn_exp2f(gq * rsn));
;                             o[4 * n + e] = (gq * uq) * (sg * rs2); }
;                         else { const float g = ga * rs, up = ua * rs; o[4 * n + e] = g * fast_sigmoid(g) * up; } }
;                 if (F8) { unsigned w0 = 0u, w1 = 0u;
; #pragma unroll
;                     for (int e = 0; e < 8; ++e) o[e] = __builtin_amdgcn_fmed3f(o[e] * H8_SCALE, -448.0f, 448.0f);
;                     w0 = __builtin_amdgcn_cvt_pk_fp8_f32(o[0], o[1], w0, false); w0 = __builtin_amdgcn_cvt_pk_fp8_f32(o[2], o[3], w0, true);
;                     w1 = __builtin_amdgcn_cvt_pk_fp8_f32(o[4], o[5], w1, false); w1 = __builtin_amdgcn_cvt_pk_fp8_f32(o[6], o[7], w1, true);
;                     typedef unsigned u32x2_ __attribute__((ext_vector_type(2))); *(u32x2_*)((unsigned char*)O + off) = (u32x2_){w0, w1}; }
;                 else { u32x4 w; w.x = cvt_pk_bf16(o[0], o[1]); w.y = cvt_pk_bf16(o[2], o[3]); w.z = cvt_pk_bf16(o[4], o[5]); w.w = cvt_pk_bf16(o[6], o[7]);
;                     __builtin_nontemporal_store(w, (u32x4*)((bf16_t*)O + off)); } }
	v_pk_mul_f32 v[76:77], v[78:79], v[76:77]
	v_pk_mul_f32 v[78:79], v[82:83], v[80:81] op_sel_hi:[0,1]
	v_mul_f32_e32 v75, v70, v86
	v_pk_mul_f32 v[76:77], v[76:77], v[78:79]
	v_exp_f32_e32 v84, v75
	v_cvt_pk_bf16_f32 v75, v76, v77
	v_mul_f32_e32 v77, v71, v86
	v_exp_f32_e32 v77, v77
	v_add_f32_e32 v76, 1.0, v84
	v_cvt_f32_i32_e32 v67, v67
	v_cvt_f32_i32_e32 v66, v66
	v_add_f32_e32 v77, 1.0, v77
	v_rcp_f32_e32 v76, v76
	v_cvt_f32_i32_e32 v73, v73
	v_cvt_f32_i32_e32 v72, v72
	v_rcp_f32_e32 v77, v77
	v_pk_mul_f32 v[66:67], v[130:131], v[66:67]
	v_cvt_f32_i32_e32 v69, v69
	v_pk_mul_f32 v[72:73], v[136:137], v[72:73]
	v_pk_mul_f32 v[66:67], v[70:71], v[66:67]
	v_pk_mul_f32 v[70:71], v[82:83], v[76:77] op_sel_hi:[0,1]
	v_mul_f32_e32 v78, v72, v86
	v_pk_mul_f32 v[66:67], v[66:67], v[70:71]
	v_mul_f32_e32 v71, v73, v86
	v_exp_f32_e32 v78, v78
	v_exp_f32_e32 v71, v71
	v_cvt_f32_i32_e32 v68, v68
	v_cvt_pk_bf16_f32 v76, v66, v67
	v_add_f32_e32 v70, 1.0, v78
	v_add_f32_e32 v71, 1.0, v71
	v_rcp_f32_e32 v70, v70
	v_rcp_f32_e32 v71, v71
	v_pk_mul_f32 v[66:67], v[132:133], v[68:69]
	v_cvt_f32_i32_e32 v63, v63
	v_pk_mul_f32 v[66:67], v[72:73], v[66:67]
	v_pk_mul_f32 v[68:69], v[82:83], v[70:71] op_sel_hi:[0,1]
	v_pk_mul_f32 v[66:67], v[66:67], v[68:69]
	v_cvt_f32_i32_e32 v62, v62
	v_cvt_pk_bf16_f32 v77, v66, v67
	ds_read2_b32 v[66:67], v118 offset0:128 offset1:144
	v_mad_i64_i32 v[68:69], s[24:25], v83, s62, v[114:115]
	v_lshl_add_u64 v[68:69], v[68:69], 0, v[110:111]
	v_pk_mul_f32 v[62:63], v[142:143], v[62:63]
	s_waitcnt lgkmcnt(0)
	v_mul_f32_e32 v70, 0xbfb8aa3b, v66
	v_mul_f32_e32 v71, v62, v70
	global_store_dwordx4 v[68:69], v[74:77], off nt
	v_mul_f32_e32 v69, v63, v70
	v_exp_f32_e32 v71, v71
	v_cvt_f32_i32_e32 v59, v59
	v_cvt_f32_i32_e32 v58, v58
	v_exp_f32_e32 v69, v69
	v_cvt_f32_i32_e32 v65, v65
	v_cvt_f32_i32_e32 v64, v64
	v_add_f32_e32 v68, 1.0, v71
	v_pk_mul_f32 v[58:59], v[138:139], v[58:59]
	v_add_f32_e32 v69, 1.0, v69
	v_rcp_f32_e32 v68, v68
	v_rcp_f32_e32 v69, v69
	v_pk_mul_f32 v[58:59], v[62:63], v[58:59]
	v_pk_mul_f32 v[62:63], v[144:145], v[64:65]
	v_mul_f32_e32 v66, v66, v66
	v_mul_f32_e32 v64, v62, v70
	v_exp_f32_e32 v71, v64
	v_pk_mul_f32 v[64:65], v[66:67], v[68:69] op_sel_hi:[0,1]
	v_pk_mul_f32 v[58:59], v[58:59], v[64:65]
	v_cvt_f32_i32_e32 v61, v61
	v_cvt_pk_bf16_f32 v58, v58, v59
	v_add_f32_e32 v59, 1.0, v71
	v_rcp_f32_e32 v64, v59
	v_mul_f32_e32 v59, v63, v70
	v_exp_f32_e32 v59, v59
	v_cvt_f32_i32_e32 v60, v60
	v_cvt_f32_i32_e32 v55, v55
	v_cvt_f32_i32_e32 v54, v54
	v_add_f32_e32 v59, 1.0, v59
	v_rcp_f32_e32 v65, v59
	v_pk_mul_f32 v[60:61], v[140:141], v[60:61]
	v_pk_mul_f32 v[54:55], v[134:135], v[54:55]
	v_pk_mul_f32 v[60:61], v[62:63], v[60:61]
	v_pk_mul_f32 v[62:63], v[66:67], v[64:65] op_sel_hi:[0,1]
	v_mul_f32_e32 v59, v54, v70
	v_pk_mul_f32 v[60:61], v[60:61], v[62:63]
	v_exp_f32_e32 v68, v59
	v_cvt_pk_bf16_f32 v59, v60, v61
	v_mul_f32_e32 v61, v55, v70
	v_exp_f32_e32 v61, v61
	v_add_f32_e32 v60, 1.0, v68
	v_cvt_f32_i32_e32 v51, v51
	v_cvt_f32_i32_e32 v50, v50
	v_add_f32_e32 v61, 1.0, v61
	v_rcp_f32_e32 v60, v60
	v_cvt_f32_i32_e32 v57, v57
	v_cvt_f32_i32_e32 v56, v56
	v_rcp_f32_e32 v61, v61
	v_pk_mul_f32 v[50:51], v[130:131], v[50:51]
	v_cvt_f32_i32_e32 v53, v53
	v_pk_mul_f32 v[56:57], v[136:137], v[56:57]
	v_pk_mul_f32 v[50:51], v[54:55], v[50:51]
	v_pk_mul_f32 v[54:55], v[66:67], v[60:61] op_sel_hi:[0,1]
	v_mul_f32_e32 v62, v56, v70
	v_pk_mul_f32 v[50:51], v[50:51], v[54:55]
	v_mul_f32_e32 v55, v57, v70
	v_exp_f32_e32 v62, v62
	v_exp_f32_e32 v55, v55
	v_cvt_f32_i32_e32 v52, v52
	v_cvt_f32_i32_e32 v47, v47
	v_add_f32_e32 v54, 1.0, v62
	v_add_f32_e32 v55, 1.0, v55
	v_rcp_f32_e32 v54, v54
	v_rcp_f32_e32 v55, v55
	v_cvt_f32_i32_e32 v46, v46
	v_cvt_pk_bf16_f32 v60, v50, v51
	v_pk_mul_f32 v[50:51], v[132:133], v[52:53]
	v_pk_mul_f32 v[52:53], v[66:67], v[54:55] op_sel_hi:[0,1]
	v_pk_mul_f32 v[50:51], v[56:57], v[50:51]
	v_mul_f32_e32 v54, 0xbfb8aa3b, v67
	v_pk_mul_f32 v[46:47], v[142:143], v[46:47]
	v_pk_mul_f32 v[50:51], v[50:51], v[52:53]
	v_mul_f32_e32 v52, v46, v54
	v_mul_f32_e32 v53, v47, v54
	v_exp_f32_e32 v52, v52
	v_cvt_f32_i32_e32 v43, v43
	v_cvt_f32_i32_e32 v42, v42
	v_exp_f32_e32 v53, v53
	v_cvt_f32_i32_e32 v49, v49
	v_cvt_f32_i32_e32 v48, v48
	v_add_f32_e32 v52, 1.0, v52
	v_pk_mul_f32 v[42:43], v[138:139], v[42:43]
	v_add_f32_e32 v53, 1.0, v53
	v_add_u32_e32 v72, 0x80, v168
	v_rcp_f32_e32 v52, v52
	v_rcp_f32_e32 v53, v53
	v_pk_mul_f32 v[42:43], v[46:47], v[42:43]
	v_pk_mul_f32 v[46:47], v[144:145], v[48:49]
	v_cvt_pk_bf16_f32 v61, v50, v51
	v_mad_i64_i32 v[50:51], s[24:25], v72, s62, v[114:115]
	v_mul_f32_e32 v48, v46, v54
	v_lshl_add_u64 v[50:51], v[50:51], 0, v[110:111]
	v_exp_f32_e32 v55, v48
	global_store_dwordx4 v[50:51], v[58:61], off nt
	v_add_u32_e32 v51, 0x90, v168
	v_mul_f32_e32 v50, v67, v67
	v_pk_mul_f32 v[48:49], v[50:51], v[52:53] op_sel_hi:[0,1]
	v_pk_mul_f32 v[42:43], v[42:43], v[48:49]
	v_cvt_f32_i32_e32 v45, v45
	v_cvt_pk_bf16_f32 v42, v42, v43
	v_add_f32_e32 v43, 1.0, v55
	v_rcp_f32_e32 v48, v43
	v_mul_f32_e32 v43, v47, v54
	v_exp_f32_e32 v43, v43
	v_cvt_f32_i32_e32 v44, v44
	v_cvt_f32_i32_e32 v39, v39
	v_cvt_f32_i32_e32 v38, v38
	v_add_f32_e32 v43, 1.0, v43
	v_rcp_f32_e32 v49, v43
	v_pk_mul_f32 v[44:45], v[140:141], v[44:45]
	v_pk_mul_f32 v[38:39], v[134:135], v[38:39]
	v_pk_mul_f32 v[44:45], v[46:47], v[44:45]
	v_pk_mul_f32 v[46:47], v[50:51], v[48:49] op_sel_hi:[0,1]
	v_mul_f32_e32 v43, v38, v54
	v_pk_mul_f32 v[44:45], v[44:45], v[46:47]
	v_exp_f32_e32 v52, v43
	v_cvt_pk_bf16_f32 v43, v44, v45
	v_mul_f32_e32 v45, v39, v54
	v_exp_f32_e32 v45, v45
	v_add_f32_e32 v44, 1.0, v52
	v_cvt_f32_i32_e32 v35, v35
	v_cvt_f32_i32_e32 v34, v34
	v_add_f32_e32 v45, 1.0, v45
	v_rcp_f32_e32 v44, v44
	v_cvt_f32_i32_e32 v41, v41
	v_cvt_f32_i32_e32 v40, v40
	v_rcp_f32_e32 v45, v45
	v_pk_mul_f32 v[34:35], v[130:131], v[34:35]
	v_cvt_f32_i32_e32 v37, v37
	v_pk_mul_f32 v[40:41], v[136:137], v[40:41]
	v_pk_mul_f32 v[34:35], v[38:39], v[34:35]
	v_pk_mul_f32 v[38:39], v[50:51], v[44:45] op_sel_hi:[0,1]
	v_mul_f32_e32 v46, v40, v54
	v_pk_mul_f32 v[34:35], v[34:35], v[38:39]
	v_mul_f32_e32 v39, v41, v54
	v_exp_f32_e32 v46, v46
	v_exp_f32_e32 v39, v39
	v_cvt_f32_i32_e32 v36, v36
	v_cvt_pk_bf16_f32 v44, v34, v35
	v_add_f32_e32 v38, 1.0, v46
	v_add_f32_e32 v39, 1.0, v39
	v_rcp_f32_e32 v38, v38
	v_rcp_f32_e32 v39, v39
	v_pk_mul_f32 v[34:35], v[132:133], v[36:37]
	v_cvt_f32_i32_e32 v31, v31
	v_pk_mul_f32 v[34:35], v[40:41], v[34:35]
	v_pk_mul_f32 v[36:37], v[50:51], v[38:39] op_sel_hi:[0,1]
	v_pk_mul_f32 v[34:35], v[34:35], v[36:37]
	v_cvt_f32_i32_e32 v30, v30
	v_cvt_pk_bf16_f32 v45, v34, v35
	ds_read2_b32 v[34:35], v118 offset0:160 offset1:176
	v_mad_i64_i32 v[36:37], s[24:25], v51, s62, v[114:115]
	v_lshl_add_u64 v[36:37], v[36:37], 0, v[110:111]
	v_pk_mul_f32 v[30:31], v[142:143], v[30:31]
	s_waitcnt lgkmcnt(0)
; __device__ __forceinline__ float fast_sigmoid(float x) { return __builtin_amdgcn_rcpf(1.0f + __expf(-x)); }
;     __device__ __forceinline__ void operator()(const f32x4 (&acc)[2][2][4][2], const Unit& u, int wr, int wc, int fr, int fq) const {
;     ...
;             for (int m = 0; m < 4; ++m) { const size_t off = (size_t)(row0 + ai * HALF + m * 16) * ldc + col0;
;                 const float rs = IN8 ? rt.tab[sl * 256 + wr * 64 + ai * HALF + m * 16 + fr] : isc;
;                 const float rsn = rs * -1.4426950408889634f, rs2 = rs * rs; (void)rsn; (void)rs2;
;                 float o[8];
; #pragma unroll
;                 for (int n = 0; n < 2; ++n)
; #pragma unroll
;                     for (int e = 0; e < 4; ++e) { const float ga = acc[ai][0][m][n][e], ua = acc[ai][1][m][n][e];
;                         if (IN8) {
;                             const float gq = (float)__float_as_int(ga) * cg[n][e], uq = (float)__float_as_int(ua) * cu[n][e];
;                             const float sg = __builtin_amdgcn_rcpf(1.0f + __builtin_amdgcn_exp2f(gq * rsn));
;                             o[4 * n + e] = (gq * uq) * (sg * rs2); }
;                         else { const float g = ga * rs, up = ua * rs; o[4 * n + e] = g * fast_sigmoid(g) * up; } }
;                 if (F8) { unsigned w0 = 0u, w1 = 0u;
; #pragma unroll
;                     for (int e = 0; e < 8; ++e) o[e] = __builtin_amdgcn_fmed3f(o[e] * H8_SCALE, -448.0f, 448.0f);
;                     w0 = __builtin_amdgcn_cvt_pk_fp8_f32(o[0], o[1], w0, false); w0 = __builtin_amdgcn_cvt_pk_fp8_f32(o[2], o[3], w0, true);
;                     w1 = __builtin_amdgcn_cvt_pk_fp8_f32(o[4], o[5], w1, false); w1 = __builtin_amdgcn_cvt_pk_fp8_f32(o[6], o[7], w1, true);
;                     typedef unsigned u32x2_ __attribute__((ext_vector_type(2))); *(u32x2_*)((unsigned char*)O + off) = (u32x2_){w0, w1}; }
;                 else { u32x4 w; w.x = cvt_pk_bf16(o[0], o[1]); w.y = cvt_pk_bf16(o[2], o[3]); w.z = cvt_pk_bf16(o[4], o[5]); w.w = cvt_pk_bf16(o[6], o[7]);
;                     __builtin_nontemporal_store(w, (u32x4*)((bf16_t*)O + off)); } }
	v_mul_f32_e32 v38, 0xbfb8aa3b, v34
	v_mul_f32_e32 v39, v30, v38
	global_store_dwordx4 v[36:37], v[42:45], off nt
	v_mul_f32_e32 v37, v31, v38
	v_exp_f32_e32 v39, v39
	v_cvt_f32_i32_e32 v27, v27
	v_cvt_f32_i32_e32 v26, v26
	v_exp_f32_e32 v37, v37
	v_cvt_f32_i32_e32 v33, v33
	v_cvt_f32_i32_e32 v32, v32
	v_add_f32_e32 v36, 1.0, v39
	v_pk_mul_f32 v[26:27], v[138:139], v[26:27]
	v_add_f32_e32 v37, 1.0, v37
	v_rcp_f32_e32 v36, v36
	v_rcp_f32_e32 v37, v37
	v_pk_mul_f32 v[26:27], v[30:31], v[26:27]
	v_pk_mul_f32 v[30:31], v[144:145], v[32:33]
	v_mul_f32_e32 v34, v34, v34
	v_mul_f32_e32 v32, v30, v38
	v_exp_f32_e32 v39, v32
	v_pk_mul_f32 v[32:33], v[34:35], v[36:37] op_sel_hi:[0,1]
	v_pk_mul_f32 v[26:27], v[26:27], v[32:33]
	v_cvt_f32_i32_e32 v29, v29
	v_cvt_pk_bf16_f32 v26, v26, v27
	v_add_f32_e32 v27, 1.0, v39
	v_rcp_f32_e32 v32, v27
	v_mul_f32_e32 v27, v31, v38
	v_exp_f32_e32 v27, v27
	v_cvt_f32_i32_e32 v28, v28
	v_cvt_f32_i32_e32 v23, v23
	v_cvt_f32_i32_e32 v22, v22
	v_add_f32_e32 v27, 1.0, v27
	v_rcp_f32_e32 v33, v27
	v_pk_mul_f32 v[28:29], v[140:141], v[28:29]
	v_pk_mul_f32 v[22:23], v[134:135], v[22:23]
	v_pk_mul_f32 v[28:29], v[30:31], v[28:29]
	v_pk_mul_f32 v[30:31], v[34:35], v[32:33] op_sel_hi:[0,1]
	v_mul_f32_e32 v27, v22, v38
	v_pk_mul_f32 v[28:29], v[28:29], v[30:31]
	v_exp_f32_e32 v36, v27
	v_cvt_pk_bf16_f32 v27, v28, v29
	v_mul_f32_e32 v29, v23, v38
	v_exp_f32_e32 v29, v29
	v_add_f32_e32 v28, 1.0, v36
	v_cvt_f32_i32_e32 v19, v19
	v_cvt_f32_i32_e32 v18, v18
	v_add_f32_e32 v29, 1.0, v29
	v_rcp_f32_e32 v28, v28
	v_cvt_f32_i32_e32 v25, v25
	v_cvt_f32_i32_e32 v24, v24
	v_rcp_f32_e32 v29, v29
	v_pk_mul_f32 v[18:19], v[130:131], v[18:19]
	v_cvt_f32_i32_e32 v21, v21
	v_pk_mul_f32 v[24:25], v[136:137], v[24:25]
	v_pk_mul_f32 v[18:19], v[22:23], v[18:19]
	v_pk_mul_f32 v[22:23], v[34:35], v[28:29] op_sel_hi:[0,1]
	v_mul_f32_e32 v30, v24, v38
	v_pk_mul_f32 v[18:19], v[18:19], v[22:23]
	v_mul_f32_e32 v23, v25, v38
	v_exp_f32_e32 v30, v30
	v_exp_f32_e32 v23, v23
	v_cvt_f32_i32_e32 v20, v20
	v_cvt_f32_i32_e32 v15, v15
	v_add_f32_e32 v22, 1.0, v30
	v_add_f32_e32 v23, 1.0, v23
	v_rcp_f32_e32 v22, v22
	v_rcp_f32_e32 v23, v23
	v_cvt_f32_i32_e32 v14, v14
	v_cvt_pk_bf16_f32 v28, v18, v19
	v_pk_mul_f32 v[18:19], v[132:133], v[20:21]
	v_pk_mul_f32 v[20:21], v[34:35], v[22:23] op_sel_hi:[0,1]
	v_pk_mul_f32 v[18:19], v[24:25], v[18:19]
	v_mul_f32_e32 v22, 0xbfb8aa3b, v35
	v_pk_mul_f32 v[14:15], v[142:143], v[14:15]
	v_pk_mul_f32 v[18:19], v[18:19], v[20:21]
	v_mul_f32_e32 v20, v14, v22
	v_mul_f32_e32 v21, v15, v22
	v_exp_f32_e32 v20, v20
	v_cvt_f32_i32_e32 v11, v11
	v_cvt_f32_i32_e32 v10, v10
	v_exp_f32_e32 v21, v21
	v_cvt_f32_i32_e32 v17, v17
	v_cvt_f32_i32_e32 v16, v16
	v_add_f32_e32 v20, 1.0, v20
	v_pk_mul_f32 v[10:11], v[138:139], v[10:11]
	v_add_f32_e32 v21, 1.0, v21
	v_add_u32_e32 v40, 0xa0, v168
	v_rcp_f32_e32 v20, v20
	v_rcp_f32_e32 v21, v21
	v_pk_mul_f32 v[10:11], v[14:15], v[10:11]
	v_pk_mul_f32 v[14:15], v[144:145], v[16:17]
	v_cvt_pk_bf16_f32 v29, v18, v19
	v_mad_i64_i32 v[18:19], s[24:25], v40, s62, v[114:115]
	v_mul_f32_e32 v16, v14, v22
	v_lshl_add_u64 v[18:19], v[18:19], 0, v[110:111]
	v_exp_f32_e32 v23, v16
	global_store_dwordx4 v[18:19], v[26:29], off nt
	v_add_u32_e32 v19, 0xb0, v168
	v_mul_f32_e32 v18, v35, v35
	v_pk_mul_f32 v[16:17], v[18:19], v[20:21] op_sel_hi:[0,1]
	v_pk_mul_f32 v[10:11], v[10:11], v[16:17]
	v_cvt_f32_i32_e32 v13, v13
	v_cvt_pk_bf16_f32 v10, v10, v11
	v_add_f32_e32 v11, 1.0, v23
	v_rcp_f32_e32 v16, v11
	v_mul_f32_e32 v11, v15, v22
	v_exp_f32_e32 v11, v11
	v_cvt_f32_i32_e32 v12, v12
	v_cvt_f32_i32_e32 v7, v7
	v_cvt_f32_i32_e32 v6, v6
	v_add_f32_e32 v11, 1.0, v11
	v_rcp_f32_e32 v17, v11
	v_pk_mul_f32 v[12:13], v[140:141], v[12:13]
	v_pk_mul_f32 v[6:7], v[134:135], v[6:7]
	v_pk_mul_f32 v[12:13], v[14:15], v[12:13]
	v_pk_mul_f32 v[14:15], v[18:19], v[16:17] op_sel_hi:[0,1]
	v_mul_f32_e32 v11, v6, v22
	v_pk_mul_f32 v[12:13], v[12:13], v[14:15]
	v_exp_f32_e32 v20, v11
	v_cvt_pk_bf16_f32 v11, v12, v13
	v_mul_f32_e32 v13, v7, v22
	v_exp_f32_e32 v13, v13
	v_add_f32_e32 v12, 1.0, v20
	v_cvt_f32_i32_e32 v3, v3
	v_cvt_f32_i32_e32 v2, v2
	v_add_f32_e32 v13, 1.0, v13
	v_rcp_f32_e32 v12, v12
	v_cvt_f32_i32_e32 v9, v9
	v_cvt_f32_i32_e32 v8, v8
	v_rcp_f32_e32 v13, v13
	v_pk_mul_f32 v[2:3], v[130:131], v[2:3]
	v_cvt_f32_i32_e32 v5, v5
	v_pk_mul_f32 v[8:9], v[136:137], v[8:9]
	v_pk_mul_f32 v[2:3], v[6:7], v[2:3]
	v_pk_mul_f32 v[6:7], v[18:19], v[12:13] op_sel_hi:[0,1]
	v_mul_f32_e32 v14, v8, v22
	v_pk_mul_f32 v[2:3], v[2:3], v[6:7]
	v_mul_f32_e32 v7, v9, v22
	v_exp_f32_e32 v14, v14
	v_exp_f32_e32 v7, v7
	v_cvt_f32_i32_e32 v4, v4
	v_cvt_pk_bf16_f32 v12, v2, v3
	v_add_f32_e32 v6, 1.0, v14
	v_add_f32_e32 v7, 1.0, v7
	v_rcp_f32_e32 v6, v6
	v_rcp_f32_e32 v7, v7
	v_pk_mul_f32 v[2:3], v[132:133], v[4:5]
	s_andn2_b64 vcc, exec, s[0:1]
	v_pk_mul_f32 v[2:3], v[8:9], v[2:3]
	v_pk_mul_f32 v[4:5], v[18:19], v[6:7] op_sel_hi:[0,1]
	v_pk_mul_f32 v[2:3], v[2:3], v[4:5]
	s_mov_b64 s[0:1], -1
	v_cvt_pk_bf16_f32 v13, v2, v3
	v_mad_i64_i32 v[2:3], s[24:25], v19, s62, v[114:115]
	v_lshl_add_u64 v[2:3], v[2:3], 0, v[110:111]
	global_store_dwordx4 v[2:3], v[10:13], off nt
	s_cbranch_vccnz .LBB0_222
	s_andn2_b64 vcc, exec, s[4:5]
	s_cbranch_vccnz .LBB0_221
	s_barrier
	s_branch .LBB0_221
